# early-3-tiles prologue + ring loop + nt policy on k_prep one-shot loads and stores
# baseline (speedup 1.0000x reference)
.LBB0_3:
	s_movk_i32 s3, 0xff
	s_lshl_b32 s6, s2, 8
	v_lshlrev_b32_e32 v2, 2, v0
	v_cmp_lt_u32_e32 vcc, s3, v0
	v_add_u32_e32 v1, s6, v2
	s_and_saveexec_b64 s[8:9], vcc
	s_xor_b64 s[8:9], exec, s[8:9]
	s_cbranch_execz .LBB0_5
	s_load_dwordx2 s[10:11], s[0:1], 0x0
	s_load_dwordx2 s[12:13], s[0:1], 0x30
	s_ashr_i32 s7, s6, 31
	v_mov_b32_e32 v3, 0
	v_lshl_add_u64 v[4:5], v[2:3], 0, s[6:7]
	s_waitcnt lgkmcnt(0)
	v_lshl_add_u64 v[4:5], v[4:5], 2, s[10:11]
	global_load_dwordx4 v[4:7], v[4:5], off offset:-4096 nt
	v_add_u32_e32 v1, 0xfffffc00, v1
	v_bfe_u32 v3, v0, 3, 3
	s_mov_b32 s3, 0x7ffff8
	v_lshrrev_b32_e32 v8, 9, v1
	v_lshlrev_b32_e32 v0, 3, v0
	v_and_or_b32 v3, v8, s3, v3
	v_and_b32_e32 v0, 48, v0
	v_bfe_u32 v1, v1, 8, 4
	v_lshlrev_b32_e32 v3, 6, v3
	v_and_b32_e32 v2, 4, v2
	v_or3_b32 v0, v3, v0, v1
	v_lshl_or_b32 v0, v0, 3, v2
	v_ashrrev_i32_e32 v1, 31, v0
	v_lshl_add_u64 v[0:1], v[0:1], 1, s[12:13]
	s_waitcnt vmcnt(0)
	v_cvt_pk_f16_f32 v3, v6, v7
	v_cvt_pk_f16_f32 v2, v4, v5
	global_store_dwordx2 v[0:1], v[2:3], off nt
.LBB0_5:
	s_andn2_saveexec_b64 s[8:9], s[8:9]
	s_cbranch_execz .LBB0_7
	s_load_dwordx2 s[10:11], s[0:1], 0x8
	s_load_dwordx2 s[12:13], s[0:1], 0x38
	s_ashr_i32 s7, s6, 31
	v_mov_b32_e32 v3, 0
	v_lshl_add_u64 v[4:5], v[2:3], 0, s[6:7]
	s_waitcnt lgkmcnt(0)
	v_lshl_add_u64 v[4:5], v[4:5], 2, s[10:11]
	global_load_dwordx4 v[4:7], v[4:5], off offset:-3072 nt
	v_add_u32_e32 v1, 0xfffffd00, v1
	v_and_b32_e32 v8, 60, v0
	v_lshrrev_b32_e32 v9, 13, v1
	v_lshrrev_b32_e32 v10, 7, v1
	v_and_or_b32 v8, v9, 3, v8
	v_and_b32_e32 v9, 48, v10
	v_and_b32_e32 v0, 0xffff8000, v1
	v_lshl_or_b32 v8, v8, 6, v9
	v_bfe_u32 v11, v1, 8, 3
	v_ashrrev_i32_e32 v1, 31, v0
	v_and_or_b32 v2, v2, 12, v8
	v_lshl_add_u64 v[0:1], v[0:1], 1, s[12:13]
	v_lshl_or_b32 v2, v2, 3, v11
	v_lshl_add_u64 v[0:1], v[2:3], 1, v[0:1]
	s_waitcnt vmcnt(0)
	v_cvt_f16_f32_e32 v2, v4
	v_cvt_f16_f32_e32 v3, v5
	v_cvt_f16_f32_e32 v4, v6
	v_cvt_f16_f32_e32 v5, v7
	global_store_short v[0:1], v2, off nt
	global_store_short v[0:1], v3, off offset:16 nt
	global_store_short v[0:1], v4, off offset:32 nt
	global_store_short v[0:1], v5, off offset:48 nt

.LBB0_18:
	s_or_b64 exec, exec, s[2:3]
	v_ashrrev_i32_e32 v1, 31, v0
	v_lshl_add_u64 v[4:5], v[0:1], 2, v[4:5]
	global_load_dwordx4 v[8:11], v[4:5], off nt
	v_cvt_f32_u32_e32 v4, v6
	v_sub_u32_e32 v7, 0, v6
	v_sub_u32_e32 v5, 0, v0
	v_max_i32_e32 v5, v0, v5
	v_rcp_iflag_f32_e32 v4, v4
	v_lshrrev_b32_e32 v12, 5, v6
	v_lshlrev_b32_e32 v13, 1, v0
	v_and_b32_e32 v14, 7, v0
	v_mul_f32_e32 v4, 0x4f7ffffe, v4
	v_cvt_u32_f32_e32 v4, v4
	v_and_b32_e32 v13, 48, v13
	v_lshl_add_u64 v[2:3], v[2:3], 1, s[4:5]
	v_mul_lo_u32 v7, v7, v4
	v_mul_hi_u32 v7, v4, v7
	v_add_u32_e32 v4, v4, v7
	v_mul_hi_u32 v4, v5, v4
	v_mul_lo_u32 v7, v4, v6
	v_sub_u32_e32 v5, v5, v7
	v_add_u32_e32 v15, 1, v4
	v_cmp_ge_u32_e32 vcc, v5, v6
	v_sub_u32_e32 v7, v5, v6
	s_nop 0
	v_cndmask_b32_e32 v4, v4, v15, vcc
	v_cndmask_b32_e32 v5, v5, v7, vcc
	v_add_u32_e32 v7, 1, v4
	v_cmp_ge_u32_e32 vcc, v5, v6
	s_nop 1
	v_cndmask_b32_e32 v4, v4, v7, vcc
	v_xor_b32_e32 v4, v4, v1
	v_sub_u32_e32 v1, v4, v1
	v_mul_lo_u32 v4, v1, v6
	v_lshrrev_b32_e32 v5, 4, v1
	v_sub_u32_e32 v0, v0, v4
	v_mul_lo_u32 v4, v5, v12
	v_lshrrev_b32_e32 v0, 5, v0
	v_and_b32_e32 v1, 15, v1
	v_add_lshl_u32 v0, v0, v4, 6
	v_or3_b32 v0, v0, v13, v1
	v_lshl_or_b32 v0, v0, 3, v14
	v_ashrrev_i32_e32 v1, 31, v0
	v_lshl_add_u64 v[0:1], v[0:1], 1, v[2:3]
	s_waitcnt vmcnt(0)
	v_cvt_pk_f16_f32 v5, v10, v11
	v_cvt_pk_f16_f32 v4, v8, v9
	global_store_dwordx2 v[0:1], v[4:5], off nt
	s_endpgm
